# norm2 phase hand-written: 2 rows/iteration share LDS router weights ([col][expert] layout, ds_write_b128 fill), packed f32 FMA router with op_sel broadcast, v_cvt_pk_bf16, fused 2-row wave reductions;
# speedup vs baseline: 1.0106x; 1.0065x over previous
.LBB0_1047:
	s_or_b64 exec, exec, s[0:1]
	s_mov_b64 s[12:13], s[72:73]
	v_mov_b32_e32 v18, v0
	s_waitcnt lgkmcnt(0)
	s_barrier
	s_nop 0
	v_cmp_gt_i32_e32 vcc, s53, v18
	v_lshlrev_b32_e32 v4, 2, v18
	s_and_saveexec_b64 s[0:1], vcc
	s_cbranch_execz .LBB0_1050
	s_load_dwordx2 s[4:5], s[12:13], 0xe8
	v_readlane_b32 s6, v255, 6
	v_readlane_b32 s7, v255, 7
	v_lshlrev_b32_e32 v2, 4, v18
	v_and_b32_e32 v3, 15, v18
	v_lshrrev_b32_e32 v5, 4, v18
	v_lshlrev_b32_e32 v3, 10, v3
	v_lshl_or_b32 v3, v5, 4, v3
	s_waitcnt lgkmcnt(0)
	s_add_u32 s4, s4, s6
	s_addc_u32 s5, s5, s7
	global_load_dwordx4 v[40:43], v2, s[4:5]
	s_add_u32 s4, s4, 0x2000
	s_addc_u32 s5, s5, 0
	global_load_dwordx4 v[44:47], v2, s[4:5]
	s_add_u32 s4, s4, 0x2000
	s_addc_u32 s5, s5, 0
	global_load_dwordx4 v[48:51], v2, s[4:5]
	s_add_u32 s4, s4, 0x2000
	s_addc_u32 s5, s5, 0
	global_load_dwordx4 v[52:55], v2, s[4:5]
	s_add_u32 s4, s4, 0x2000
	s_addc_u32 s5, s5, 0
	global_load_dwordx4 v[56:59], v2, s[4:5]
	s_add_u32 s4, s4, 0x2000
	s_addc_u32 s5, s5, 0
	global_load_dwordx4 v[60:63], v2, s[4:5]
	s_add_u32 s4, s4, 0x2000
	s_addc_u32 s5, s5, 0
	global_load_dwordx4 v[64:67], v2, s[4:5]
	s_add_u32 s4, s4, 0x2000
	s_addc_u32 s5, s5, 0
	global_load_dwordx4 v[68:71], v2, s[4:5]
	s_waitcnt vmcnt(7)
	ds_write_b128 v3, v[40:43] offset:0
	s_waitcnt vmcnt(6)
	ds_write_b128 v3, v[44:47] offset:512
	s_waitcnt vmcnt(5)
	ds_write_b128 v3, v[48:51] offset:16384
	s_waitcnt vmcnt(4)
	ds_write_b128 v3, v[52:55] offset:16896
	s_waitcnt vmcnt(3)
	ds_write_b128 v3, v[56:59] offset:32768
	s_waitcnt vmcnt(2)
	ds_write_b128 v3, v[60:63] offset:33280
	s_waitcnt vmcnt(1)
	ds_write_b128 v3, v[64:67] offset:49152
	s_waitcnt vmcnt(0)
	ds_write_b128 v3, v[68:71] offset:49664
.LBB0_1050:
	s_or_b64 exec, exec, s[0:1]
	s_abs_i32 s0, s94
	v_cvt_f32_u32_e32 v3, s0
	s_sub_i32 s5, 0, s0
	s_add_i32 s1, s24, s94
	s_add_i32 s1, s1, -1
	v_rcp_iflag_f32_e32 v3, v3
	s_xor_b32 s4, s1, s94
	s_abs_i32 s1, s1
	s_ashr_i32 s4, s4, 31
	v_mul_f32_e32 v3, 0x4f7ffffe, v3
	v_cvt_u32_f32_e32 v3, v3
	v_ashrrev_i32_e32 v2, 6, v18
	s_waitcnt lgkmcnt(0)
	s_barrier
	v_readfirstlane_b32 s6, v3
	s_mul_i32 s5, s5, s6
	s_mul_hi_u32 s5, s6, s5
	s_add_i32 s6, s6, s5
	s_mul_hi_u32 s5, s1, s6
	s_mul_i32 s6, s5, s0
	s_sub_i32 s1, s1, s6
	s_add_i32 s6, s5, 1
	s_sub_i32 s7, s1, s0
	s_cmp_ge_u32 s1, s0
	s_cselect_b32 s5, s6, s5
	s_cselect_b32 s1, s7, s1
	s_add_i32 s6, s5, 1
	s_cmp_ge_u32 s1, s0
	s_cselect_b32 s0, s6, s5
	s_xor_b32 s0, s0, s4
	s_mov_b32 s1, s2
	s_sub_i32 s0, s0, s4
	s_nop 0
	v_lshl_add_u32 v2, s1, 3, v2
	s_waitcnt vmcnt(7)
	v_mul_lo_u32 v34, v2, s0
	v_add_u32_e32 v2, s0, v34
	v_min_i32_e32 v122, s24, v2
	v_cmp_lt_i32_e32 vcc, v34, v122
	s_and_saveexec_b64 s[14:15], vcc
	s_mov_b64 s[94:95], 0x40000
	s_cbranch_execz .LBB0_1057
	v_readfirstlane_b32 s18, v34
	v_readfirstlane_b32 s19, v122
	v_readlane_b32 s20, v255, 12
	s_load_dwordx2 s[4:5], s[12:13], 0x178
	s_load_dwordx2 s[6:7], s[12:13], 0x130
	s_load_dwordx2 s[8:9], s[12:13], 0x228
	s_load_dwordx2 s[10:11], s[12:13], 0x120
	s_load_dwordx2 s[32:33], s[12:13], 0x38
	s_load_dwordx2 s[34:35], s[12:13], 0xf0
	v_and_b32_e32 v229, 63, v18
	v_lshlrev_b32_e32 v230, 3, v229
	v_lshlrev_b32_e32 v231, 4, v229
	v_bfe_u32 v232, v18, 2, 4
	v_lshlrev_b32_e32 v232, 2, v232
	v_and_b32_e32 v233, 8, v18
	v_cmp_eq_u32_e64 s[26:27], 0, v233
	v_and_b32_e32 v233, 4, v18
	v_cmp_eq_u32_e64 s[28:29], 0, v233
	v_and_b32_e32 v233, 3, v18
	v_cmp_eq_u32_e64 s[30:31], 0, v233
	v_mov_b32_e32 v234, 0x358637bd
	s_mov_b32 s25, 0xffff0000
	s_mul_i32 s16, s20, 9
	s_mov_b32 s17, 0
	s_movk_i32 s22, 0x6000
	s_mul_i32 s21, s16, s22
	s_lshl_b32 s0, s20, 12
	s_lshl_b32 s1, s20, 6
	s_lshl_b32 s23, s18, 11
	s_lshl_b32 s36, s18, 6
	s_waitcnt lgkmcnt(0)
	s_add_u32 s10, s10, s21
	s_addc_u32 s11, s11, 0
	s_add_u32 s32, s32, s0
	s_addc_u32 s33, s33, 0
	s_add_u32 s34, s34, s1
	s_addc_u32 s35, s35, 0
	s_add_u32 s4, s4, s23
	s_addc_u32 s5, s5, 0
	s_add_u32 s6, s6, s23
	s_addc_u32 s7, s7, 0
	s_add_u32 s8, s8, s36
	s_addc_u32 s9, s9, 0
	global_load_dwordx4 v[172:175], v231, s[32:33] offset:0
	global_load_dwordx4 v[176:179], v231, s[32:33] offset:1024
	global_load_dwordx4 v[180:183], v231, s[32:33] offset:2048
	global_load_dwordx4 v[184:187], v231, s[32:33] offset:3072
	global_load_dword v235, v232, s[34:35]
	s_mov_b32 s20, -1
	s_add_i32 s23, s18, 1
	s_cmp_lt_i32 s23, s19
	s_cselect_b32 s21, 1, 0
	s_bitcmp0_b32 s18, 0
	s_cselect_b32 s21, s21, 0
	s_lshl_b32 s23, s21, 11
	s_lshl_b32 s36, s21, 6
	v_add_u32_e32 v236, s23, v230
	v_add_u32_e32 v238, s23, v230
	v_add_u32_e32 v237, s36, v232
	global_load_dwordx2 v[2:3], v230, s[4:5] offset:0
	global_load_dwordx2 v[4:5], v230, s[4:5] offset:512
	global_load_dwordx2 v[6:7], v230, s[4:5] offset:1024
	global_load_dwordx2 v[8:9], v230, s[4:5] offset:1536
	global_load_dwordx2 v[10:11], v236, s[4:5] offset:0
	global_load_dwordx2 v[12:13], v236, s[4:5] offset:512
	global_load_dwordx2 v[14:15], v236, s[4:5] offset:1024
	global_load_dwordx2 v[16:17], v236, s[4:5] offset:1536
.Ln2_loop:
	ds_read_b128 v[116:119], v231 offset:0
	ds_read_b128 v[120:123], v231 offset:1024
	ds_read_b128 v[124:127], v231 offset:2048
	ds_read_b128 v[128:131], v231 offset:3072
	ds_read_b128 v[132:135], v231 offset:4096
	ds_read_b128 v[136:139], v231 offset:5120
	ds_read_b128 v[140:143], v231 offset:6144
	ds_read_b128 v[144:147], v231 offset:7168
	s_lshr_b32 s23, s18, 12
	s_cmp_lt_i32 s18, 0x8000
	s_cselect_b32 s23, s23, 8
	s_cmp_eq_u32 s23, s20
	s_cbranch_scc0 .Ln2_reload
.Ln2_reload_back:
	s_waitcnt vmcnt(10)
	v_lshlrev_b32_e32 v20, 16, v2
	v_and_b32_e32 v21, s25, v2
	v_lshlrev_b32_e32 v22, 16, v3
	v_and_b32_e32 v23, s25, v3
	v_lshlrev_b32_e32 v24, 16, v4
	v_and_b32_e32 v25, s25, v4
	v_lshlrev_b32_e32 v26, 16, v5
	v_and_b32_e32 v27, s25, v5
	v_lshlrev_b32_e32 v28, 16, v6
	v_and_b32_e32 v29, s25, v6
	v_lshlrev_b32_e32 v30, 16, v7
	v_and_b32_e32 v31, s25, v7
	v_lshlrev_b32_e32 v32, 16, v8
	v_and_b32_e32 v33, s25, v8
	v_lshlrev_b32_e32 v34, 16, v9
	v_and_b32_e32 v35, s25, v9
	v_lshlrev_b32_e32 v36, 16, v10
	v_and_b32_e32 v37, s25, v10
	v_lshlrev_b32_e32 v38, 16, v11
	v_and_b32_e32 v39, s25, v11
	v_lshlrev_b32_e32 v40, 16, v12
	v_and_b32_e32 v41, s25, v12
	v_lshlrev_b32_e32 v42, 16, v13
	v_and_b32_e32 v43, s25, v13
	v_lshlrev_b32_e32 v44, 16, v14
	v_and_b32_e32 v45, s25, v14
	v_lshlrev_b32_e32 v46, 16, v15
	v_and_b32_e32 v47, s25, v15
	v_lshlrev_b32_e32 v48, 16, v16
	v_and_b32_e32 v49, s25, v16
	v_lshlrev_b32_e32 v50, 16, v17
	v_and_b32_e32 v51, s25, v17
	s_add_i32 s36, s18, 1
	s_add_i32 s36, s36, s21
	s_cmp_ge_i32 s36, s19
	s_cbranch_scc1 .Ln2_nopf
	s_add_i32 s37, s21, 1
	s_lshl_b32 s37, s37, 11
	s_add_u32 s4, s4, s37
	s_addc_u32 s5, s5, 0
	s_add_i32 s23, s36, 1
	s_cmp_lt_i32 s23, s19
	s_cselect_b32 s37, 1, 0
	s_bitcmp0_b32 s36, 0
	s_cselect_b32 s37, s37, 0
	s_lshl_b32 s23, s37, 11
	v_add_u32_e32 v236, s23, v230
	global_load_dwordx2 v[2:3], v230, s[4:5] offset:0
	global_load_dwordx2 v[4:5], v230, s[4:5] offset:512
	global_load_dwordx2 v[6:7], v230, s[4:5] offset:1024
	global_load_dwordx2 v[8:9], v230, s[4:5] offset:1536
	global_load_dwordx2 v[10:11], v236, s[4:5] offset:0
	global_load_dwordx2 v[12:13], v236, s[4:5] offset:512
	global_load_dwordx2 v[14:15], v236, s[4:5] offset:1024
	global_load_dwordx2 v[16:17], v236, s[4:5] offset:1536
.Ln2_nopf:
	v_pk_mul_f32 v[204:205], v[20:21], v[20:21]
	v_pk_mul_f32 v[206:207], v[36:37], v[36:37]
	v_pk_fma_f32 v[204:205], v[22:23], v[22:23], v[204:205]
	v_pk_fma_f32 v[206:207], v[38:39], v[38:39], v[206:207]
	v_pk_fma_f32 v[204:205], v[24:25], v[24:25], v[204:205]
	v_pk_fma_f32 v[206:207], v[40:41], v[40:41], v[206:207]
	v_pk_fma_f32 v[204:205], v[26:27], v[26:27], v[204:205]
	v_pk_fma_f32 v[206:207], v[42:43], v[42:43], v[206:207]
	v_pk_fma_f32 v[204:205], v[28:29], v[28:29], v[204:205]
	v_pk_fma_f32 v[206:207], v[44:45], v[44:45], v[206:207]
	v_pk_fma_f32 v[204:205], v[30:31], v[30:31], v[204:205]
	v_pk_fma_f32 v[206:207], v[46:47], v[46:47], v[206:207]
	v_pk_fma_f32 v[204:205], v[32:33], v[32:33], v[204:205]
	v_pk_fma_f32 v[206:207], v[48:49], v[48:49], v[206:207]
	v_pk_fma_f32 v[204:205], v[34:35], v[34:35], v[204:205]
	v_pk_fma_f32 v[206:207], v[50:51], v[50:51], v[206:207]
	v_add_f32_e32 v204, v204, v205
	v_add_f32_e32 v206, v206, v207
	s_nop 0
	v_add_f32_dpp v204, v204, v204 quad_perm:[1,0,3,2] row_mask:0xf bank_mask:0xf bound_ctrl:1
	v_add_f32_dpp v206, v206, v206 quad_perm:[1,0,3,2] row_mask:0xf bank_mask:0xf bound_ctrl:1
	s_nop 0
	v_add_f32_dpp v204, v204, v204 quad_perm:[2,3,0,1] row_mask:0xf bank_mask:0xf bound_ctrl:1
	v_add_f32_dpp v206, v206, v206 quad_perm:[2,3,0,1] row_mask:0xf bank_mask:0xf bound_ctrl:1
	s_nop 0
	v_add_f32_dpp v204, v204, v204 row_half_mirror row_mask:0xf bank_mask:0xf bound_ctrl:1
	v_add_f32_dpp v206, v206, v206 row_half_mirror row_mask:0xf bank_mask:0xf bound_ctrl:1
	s_nop 0
	v_add_f32_dpp v204, v204, v204 row_mirror row_mask:0xf bank_mask:0xf bound_ctrl:1
	v_add_f32_dpp v206, v206, v206 row_mirror row_mask:0xf bank_mask:0xf bound_ctrl:1
	s_nop 1
	v_permlane32_swap_b32_e32 v204, v206
	v_add_f32_e32 v204, v204, v206
	v_mov_b32_e32 v206, v204
	s_nop 1
	v_permlane16_swap_b32_e32 v204, v206
	v_add_f32_e32 v204, v204, v206
	v_mov_b32_e32 v206, v204
	s_nop 1
	v_permlane32_swap_b32_e32 v204, v206
	v_fmamk_f32 v208, v204, 0x3a800000, v234
	v_fmamk_f32 v210, v206, 0x3a800000, v234
	v_rsq_f32_e32 v208, v208
	v_rsq_f32_e32 v210, v210
	v_pk_mul_f32 v[20:21], v[20:21], v[208:209] op_sel_hi:[1,0]
	v_pk_mul_f32 v[36:37], v[36:37], v[210:211] op_sel_hi:[1,0]
	v_pk_mul_f32 v[22:23], v[22:23], v[208:209] op_sel_hi:[1,0]
	v_pk_mul_f32 v[38:39], v[38:39], v[210:211] op_sel_hi:[1,0]
	v_pk_mul_f32 v[24:25], v[24:25], v[208:209] op_sel_hi:[1,0]
	v_pk_mul_f32 v[40:41], v[40:41], v[210:211] op_sel_hi:[1,0]
	v_pk_mul_f32 v[26:27], v[26:27], v[208:209] op_sel_hi:[1,0]
	v_pk_mul_f32 v[42:43], v[42:43], v[210:211] op_sel_hi:[1,0]
	v_pk_mul_f32 v[28:29], v[28:29], v[208:209] op_sel_hi:[1,0]
	v_pk_mul_f32 v[44:45], v[44:45], v[210:211] op_sel_hi:[1,0]
	v_pk_mul_f32 v[30:31], v[30:31], v[208:209] op_sel_hi:[1,0]
	v_pk_mul_f32 v[46:47], v[46:47], v[210:211] op_sel_hi:[1,0]
	v_pk_mul_f32 v[32:33], v[32:33], v[208:209] op_sel_hi:[1,0]
	v_pk_mul_f32 v[48:49], v[48:49], v[210:211] op_sel_hi:[1,0]
	v_pk_mul_f32 v[34:35], v[34:35], v[208:209] op_sel_hi:[1,0]
	v_pk_mul_f32 v[50:51], v[50:51], v[210:211] op_sel_hi:[1,0]
	v_pk_fma_f32 v[20:21], v[20:21], v[52:53], v[68:69]
	v_pk_fma_f32 v[36:37], v[36:37], v[52:53], v[68:69]
	v_pk_fma_f32 v[22:23], v[22:23], v[54:55], v[70:71]
	v_pk_fma_f32 v[38:39], v[38:39], v[54:55], v[70:71]
	v_pk_fma_f32 v[24:25], v[24:25], v[56:57], v[72:73]
	v_pk_fma_f32 v[40:41], v[40:41], v[56:57], v[72:73]
	v_pk_fma_f32 v[26:27], v[26:27], v[58:59], v[74:75]
	v_pk_fma_f32 v[42:43], v[42:43], v[58:59], v[74:75]
	v_pk_fma_f32 v[28:29], v[28:29], v[60:61], v[76:77]
	v_pk_fma_f32 v[44:45], v[44:45], v[60:61], v[76:77]
	v_pk_fma_f32 v[30:31], v[30:31], v[62:63], v[78:79]
	v_pk_fma_f32 v[46:47], v[46:47], v[62:63], v[78:79]
	v_pk_fma_f32 v[32:33], v[32:33], v[64:65], v[80:81]
	v_pk_fma_f32 v[48:49], v[48:49], v[64:65], v[80:81]
	v_pk_fma_f32 v[34:35], v[34:35], v[66:67], v[82:83]
	v_pk_fma_f32 v[50:51], v[50:51], v[66:67], v[82:83]
	v_cvt_pk_bf16_f32 v188, v20, v21
	v_cvt_pk_bf16_f32 v189, v22, v23
	v_cvt_pk_bf16_f32 v190, v24, v25
	v_cvt_pk_bf16_f32 v191, v26, v27
	v_cvt_pk_bf16_f32 v192, v28, v29
	v_cvt_pk_bf16_f32 v193, v30, v31
	v_cvt_pk_bf16_f32 v194, v32, v33
	v_cvt_pk_bf16_f32 v195, v34, v35
	v_cvt_pk_bf16_f32 v196, v36, v37
	v_cvt_pk_bf16_f32 v197, v38, v39
	v_cvt_pk_bf16_f32 v198, v40, v41
	v_cvt_pk_bf16_f32 v199, v42, v43
	v_cvt_pk_bf16_f32 v200, v44, v45
	v_cvt_pk_bf16_f32 v201, v46, v47
	v_cvt_pk_bf16_f32 v202, v48, v49
	v_cvt_pk_bf16_f32 v203, v50, v51
	global_store_dwordx2 v230, v[188:189], s[6:7] offset:0
	global_store_dwordx2 v230, v[190:191], s[6:7] offset:512
	global_store_dwordx2 v230, v[192:193], s[6:7] offset:1024
	global_store_dwordx2 v230, v[194:195], s[6:7] offset:1536
	global_store_dwordx2 v238, v[196:197], s[6:7] offset:0
	global_store_dwordx2 v238, v[198:199], s[6:7] offset:512
	global_store_dwordx2 v238, v[200:201], s[6:7] offset:1024
	global_store_dwordx2 v238, v[202:203], s[6:7] offset:1536
	ds_read_b128 v[148:151], v231 offset:8192
	ds_read_b128 v[152:155], v231 offset:9216
	ds_read_b128 v[156:159], v231 offset:10240
	ds_read_b128 v[160:163], v231 offset:11264
	s_waitcnt lgkmcnt(8)
	v_pk_mul_f32 v[84:85], v[20:21], v[116:117] op_sel_hi:[0,1]
	v_pk_mul_f32 v[86:87], v[20:21], v[118:119] op_sel_hi:[0,1]
	v_pk_mul_f32 v[88:89], v[20:21], v[120:121] op_sel_hi:[0,1]
	v_pk_mul_f32 v[90:91], v[20:21], v[122:123] op_sel_hi:[0,1]
	v_pk_mul_f32 v[92:93], v[20:21], v[124:125] op_sel_hi:[0,1]
	v_pk_mul_f32 v[94:95], v[20:21], v[126:127] op_sel_hi:[0,1]
	v_pk_mul_f32 v[96:97], v[20:21], v[128:129] op_sel_hi:[0,1]
	v_pk_mul_f32 v[98:99], v[20:21], v[130:131] op_sel_hi:[0,1]
	v_pk_mul_f32 v[100:101], v[36:37], v[116:117] op_sel_hi:[0,1]
	v_pk_mul_f32 v[102:103], v[36:37], v[118:119] op_sel_hi:[0,1]
	v_pk_mul_f32 v[104:105], v[36:37], v[120:121] op_sel_hi:[0,1]
	v_pk_mul_f32 v[106:107], v[36:37], v[122:123] op_sel_hi:[0,1]
	v_pk_mul_f32 v[108:109], v[36:37], v[124:125] op_sel_hi:[0,1]
	v_pk_mul_f32 v[110:111], v[36:37], v[126:127] op_sel_hi:[0,1]
	v_pk_mul_f32 v[112:113], v[36:37], v[128:129] op_sel_hi:[0,1]
	v_pk_mul_f32 v[114:115], v[36:37], v[130:131] op_sel_hi:[0,1]
	ds_read_b128 v[116:119], v231 offset:12288
	ds_read_b128 v[120:123], v231 offset:13312
	ds_read_b128 v[124:127], v231 offset:14336
	ds_read_b128 v[128:131], v231 offset:15360
	s_waitcnt lgkmcnt(8)
	v_pk_fma_f32 v[84:85], v[20:21], v[132:133], v[84:85] op_sel:[1,0,0]
	v_pk_fma_f32 v[86:87], v[20:21], v[134:135], v[86:87] op_sel:[1,0,0]
	v_pk_fma_f32 v[88:89], v[20:21], v[136:137], v[88:89] op_sel:[1,0,0]
	v_pk_fma_f32 v[90:91], v[20:21], v[138:139], v[90:91] op_sel:[1,0,0]
	v_pk_fma_f32 v[92:93], v[20:21], v[140:141], v[92:93] op_sel:[1,0,0]
	v_pk_fma_f32 v[94:95], v[20:21], v[142:143], v[94:95] op_sel:[1,0,0]
	v_pk_fma_f32 v[96:97], v[20:21], v[144:145], v[96:97] op_sel:[1,0,0]
	v_pk_fma_f32 v[98:99], v[20:21], v[146:147], v[98:99] op_sel:[1,0,0]
	v_pk_fma_f32 v[100:101], v[36:37], v[132:133], v[100:101] op_sel:[1,0,0]
	v_pk_fma_f32 v[102:103], v[36:37], v[134:135], v[102:103] op_sel:[1,0,0]
	v_pk_fma_f32 v[104:105], v[36:37], v[136:137], v[104:105] op_sel:[1,0,0]
	v_pk_fma_f32 v[106:107], v[36:37], v[138:139], v[106:107] op_sel:[1,0,0]
	v_pk_fma_f32 v[108:109], v[36:37], v[140:141], v[108:109] op_sel:[1,0,0]
	v_pk_fma_f32 v[110:111], v[36:37], v[142:143], v[110:111] op_sel:[1,0,0]
	v_pk_fma_f32 v[112:113], v[36:37], v[144:145], v[112:113] op_sel:[1,0,0]
	v_pk_fma_f32 v[114:115], v[36:37], v[146:147], v[114:115] op_sel:[1,0,0]
	ds_read_b128 v[132:135], v231 offset:16384
	ds_read_b128 v[136:139], v231 offset:17408
	ds_read_b128 v[140:143], v231 offset:18432
	ds_read_b128 v[144:147], v231 offset:19456
	s_waitcnt lgkmcnt(8)
	v_pk_fma_f32 v[84:85], v[22:23], v[148:149], v[84:85] op_sel_hi:[0,1,1]
	v_pk_fma_f32 v[86:87], v[22:23], v[150:151], v[86:87] op_sel_hi:[0,1,1]
	v_pk_fma_f32 v[88:89], v[22:23], v[152:153], v[88:89] op_sel_hi:[0,1,1]
	v_pk_fma_f32 v[90:91], v[22:23], v[154:155], v[90:91] op_sel_hi:[0,1,1]
	v_pk_fma_f32 v[92:93], v[22:23], v[156:157], v[92:93] op_sel_hi:[0,1,1]
	v_pk_fma_f32 v[94:95], v[22:23], v[158:159], v[94:95] op_sel_hi:[0,1,1]
	v_pk_fma_f32 v[96:97], v[22:23], v[160:161], v[96:97] op_sel_hi:[0,1,1]
	v_pk_fma_f32 v[98:99], v[22:23], v[162:163], v[98:99] op_sel_hi:[0,1,1]
	v_pk_fma_f32 v[100:101], v[38:39], v[148:149], v[100:101] op_sel_hi:[0,1,1]
	v_pk_fma_f32 v[102:103], v[38:39], v[150:151], v[102:103] op_sel_hi:[0,1,1]
	v_pk_fma_f32 v[104:105], v[38:39], v[152:153], v[104:105] op_sel_hi:[0,1,1]
	v_pk_fma_f32 v[106:107], v[38:39], v[154:155], v[106:107] op_sel_hi:[0,1,1]
	v_pk_fma_f32 v[108:109], v[38:39], v[156:157], v[108:109] op_sel_hi:[0,1,1]
	v_pk_fma_f32 v[110:111], v[38:39], v[158:159], v[110:111] op_sel_hi:[0,1,1]
	v_pk_fma_f32 v[112:113], v[38:39], v[160:161], v[112:113] op_sel_hi:[0,1,1]
	v_pk_fma_f32 v[114:115], v[38:39], v[162:163], v[114:115] op_sel_hi:[0,1,1]
	ds_read_b128 v[148:151], v231 offset:20480
	ds_read_b128 v[152:155], v231 offset:21504
	ds_read_b128 v[156:159], v231 offset:22528
	ds_read_b128 v[160:163], v231 offset:23552
	s_waitcnt lgkmcnt(8)
	v_pk_fma_f32 v[84:85], v[22:23], v[116:117], v[84:85] op_sel:[1,0,0]
	v_pk_fma_f32 v[86:87], v[22:23], v[118:119], v[86:87] op_sel:[1,0,0]
	v_pk_fma_f32 v[88:89], v[22:23], v[120:121], v[88:89] op_sel:[1,0,0]
	v_pk_fma_f32 v[90:91], v[22:23], v[122:123], v[90:91] op_sel:[1,0,0]
	v_pk_fma_f32 v[92:93], v[22:23], v[124:125], v[92:93] op_sel:[1,0,0]
	v_pk_fma_f32 v[94:95], v[22:23], v[126:127], v[94:95] op_sel:[1,0,0]
	v_pk_fma_f32 v[96:97], v[22:23], v[128:129], v[96:97] op_sel:[1,0,0]
	v_pk_fma_f32 v[98:99], v[22:23], v[130:131], v[98:99] op_sel:[1,0,0]
	v_pk_fma_f32 v[100:101], v[38:39], v[116:117], v[100:101] op_sel:[1,0,0]
	v_pk_fma_f32 v[102:103], v[38:39], v[118:119], v[102:103] op_sel:[1,0,0]
	v_pk_fma_f32 v[104:105], v[38:39], v[120:121], v[104:105] op_sel:[1,0,0]
	v_pk_fma_f32 v[106:107], v[38:39], v[122:123], v[106:107] op_sel:[1,0,0]
	v_pk_fma_f32 v[108:109], v[38:39], v[124:125], v[108:109] op_sel:[1,0,0]
	v_pk_fma_f32 v[110:111], v[38:39], v[126:127], v[110:111] op_sel:[1,0,0]
	v_pk_fma_f32 v[112:113], v[38:39], v[128:129], v[112:113] op_sel:[1,0,0]
	v_pk_fma_f32 v[114:115], v[38:39], v[130:131], v[114:115] op_sel:[1,0,0]
	ds_read_b128 v[116:119], v231 offset:24576
	ds_read_b128 v[120:123], v231 offset:25600
	ds_read_b128 v[124:127], v231 offset:26624
	ds_read_b128 v[128:131], v231 offset:27648
	s_waitcnt lgkmcnt(8)
	v_pk_fma_f32 v[84:85], v[24:25], v[132:133], v[84:85] op_sel_hi:[0,1,1]
	v_pk_fma_f32 v[86:87], v[24:25], v[134:135], v[86:87] op_sel_hi:[0,1,1]
	v_pk_fma_f32 v[88:89], v[24:25], v[136:137], v[88:89] op_sel_hi:[0,1,1]
	v_pk_fma_f32 v[90:91], v[24:25], v[138:139], v[90:91] op_sel_hi:[0,1,1]
	v_pk_fma_f32 v[92:93], v[24:25], v[140:141], v[92:93] op_sel_hi:[0,1,1]
	v_pk_fma_f32 v[94:95], v[24:25], v[142:143], v[94:95] op_sel_hi:[0,1,1]
	v_pk_fma_f32 v[96:97], v[24:25], v[144:145], v[96:97] op_sel_hi:[0,1,1]
	v_pk_fma_f32 v[98:99], v[24:25], v[146:147], v[98:99] op_sel_hi:[0,1,1]
	v_pk_fma_f32 v[100:101], v[40:41], v[132:133], v[100:101] op_sel_hi:[0,1,1]
	v_pk_fma_f32 v[102:103], v[40:41], v[134:135], v[102:103] op_sel_hi:[0,1,1]
	v_pk_fma_f32 v[104:105], v[40:41], v[136:137], v[104:105] op_sel_hi:[0,1,1]
	v_pk_fma_f32 v[106:107], v[40:41], v[138:139], v[106:107] op_sel_hi:[0,1,1]
	v_pk_fma_f32 v[108:109], v[40:41], v[140:141], v[108:109] op_sel_hi:[0,1,1]
	v_pk_fma_f32 v[110:111], v[40:41], v[142:143], v[110:111] op_sel_hi:[0,1,1]
	v_pk_fma_f32 v[112:113], v[40:41], v[144:145], v[112:113] op_sel_hi:[0,1,1]
	v_pk_fma_f32 v[114:115], v[40:41], v[146:147], v[114:115] op_sel_hi:[0,1,1]
	ds_read_b128 v[132:135], v231 offset:28672
	ds_read_b128 v[136:139], v231 offset:29696
	ds_read_b128 v[140:143], v231 offset:30720
	ds_read_b128 v[144:147], v231 offset:31744
	s_waitcnt lgkmcnt(8)
	v_pk_fma_f32 v[84:85], v[24:25], v[148:149], v[84:85] op_sel:[1,0,0]
	v_pk_fma_f32 v[86:87], v[24:25], v[150:151], v[86:87] op_sel:[1,0,0]
	v_pk_fma_f32 v[88:89], v[24:25], v[152:153], v[88:89] op_sel:[1,0,0]
	v_pk_fma_f32 v[90:91], v[24:25], v[154:155], v[90:91] op_sel:[1,0,0]
	v_pk_fma_f32 v[92:93], v[24:25], v[156:157], v[92:93] op_sel:[1,0,0]
	v_pk_fma_f32 v[94:95], v[24:25], v[158:159], v[94:95] op_sel:[1,0,0]
	v_pk_fma_f32 v[96:97], v[24:25], v[160:161], v[96:97] op_sel:[1,0,0]
	v_pk_fma_f32 v[98:99], v[24:25], v[162:163], v[98:99] op_sel:[1,0,0]
	v_pk_fma_f32 v[100:101], v[40:41], v[148:149], v[100:101] op_sel:[1,0,0]
	v_pk_fma_f32 v[102:103], v[40:41], v[150:151], v[102:103] op_sel:[1,0,0]
	v_pk_fma_f32 v[104:105], v[40:41], v[152:153], v[104:105] op_sel:[1,0,0]
	v_pk_fma_f32 v[106:107], v[40:41], v[154:155], v[106:107] op_sel:[1,0,0]
	v_pk_fma_f32 v[108:109], v[40:41], v[156:157], v[108:109] op_sel:[1,0,0]
	v_pk_fma_f32 v[110:111], v[40:41], v[158:159], v[110:111] op_sel:[1,0,0]
	v_pk_fma_f32 v[112:113], v[40:41], v[160:161], v[112:113] op_sel:[1,0,0]
	v_pk_fma_f32 v[114:115], v[40:41], v[162:163], v[114:115] op_sel:[1,0,0]
	ds_read_b128 v[148:151], v231 offset:32768
	ds_read_b128 v[152:155], v231 offset:33792
	ds_read_b128 v[156:159], v231 offset:34816
	ds_read_b128 v[160:163], v231 offset:35840
	s_waitcnt lgkmcnt(8)
	v_pk_fma_f32 v[84:85], v[26:27], v[116:117], v[84:85] op_sel_hi:[0,1,1]
	v_pk_fma_f32 v[86:87], v[26:27], v[118:119], v[86:87] op_sel_hi:[0,1,1]
	v_pk_fma_f32 v[88:89], v[26:27], v[120:121], v[88:89] op_sel_hi:[0,1,1]
	v_pk_fma_f32 v[90:91], v[26:27], v[122:123], v[90:91] op_sel_hi:[0,1,1]
	v_pk_fma_f32 v[92:93], v[26:27], v[124:125], v[92:93] op_sel_hi:[0,1,1]
	v_pk_fma_f32 v[94:95], v[26:27], v[126:127], v[94:95] op_sel_hi:[0,1,1]
	v_pk_fma_f32 v[96:97], v[26:27], v[128:129], v[96:97] op_sel_hi:[0,1,1]
	v_pk_fma_f32 v[98:99], v[26:27], v[130:131], v[98:99] op_sel_hi:[0,1,1]
	v_pk_fma_f32 v[100:101], v[42:43], v[116:117], v[100:101] op_sel_hi:[0,1,1]
	v_pk_fma_f32 v[102:103], v[42:43], v[118:119], v[102:103] op_sel_hi:[0,1,1]
	v_pk_fma_f32 v[104:105], v[42:43], v[120:121], v[104:105] op_sel_hi:[0,1,1]
	v_pk_fma_f32 v[106:107], v[42:43], v[122:123], v[106:107] op_sel_hi:[0,1,1]
	v_pk_fma_f32 v[108:109], v[42:43], v[124:125], v[108:109] op_sel_hi:[0,1,1]
	v_pk_fma_f32 v[110:111], v[42:43], v[126:127], v[110:111] op_sel_hi:[0,1,1]
	v_pk_fma_f32 v[112:113], v[42:43], v[128:129], v[112:113] op_sel_hi:[0,1,1]
	v_pk_fma_f32 v[114:115], v[42:43], v[130:131], v[114:115] op_sel_hi:[0,1,1]
	ds_read_b128 v[116:119], v231 offset:36864
	ds_read_b128 v[120:123], v231 offset:37888
	ds_read_b128 v[124:127], v231 offset:38912
	ds_read_b128 v[128:131], v231 offset:39936
	s_waitcnt lgkmcnt(8)
	v_pk_fma_f32 v[84:85], v[26:27], v[132:133], v[84:85] op_sel:[1,0,0]
	v_pk_fma_f32 v[86:87], v[26:27], v[134:135], v[86:87] op_sel:[1,0,0]
	v_pk_fma_f32 v[88:89], v[26:27], v[136:137], v[88:89] op_sel:[1,0,0]
	v_pk_fma_f32 v[90:91], v[26:27], v[138:139], v[90:91] op_sel:[1,0,0]
	v_pk_fma_f32 v[92:93], v[26:27], v[140:141], v[92:93] op_sel:[1,0,0]
	v_pk_fma_f32 v[94:95], v[26:27], v[142:143], v[94:95] op_sel:[1,0,0]
	v_pk_fma_f32 v[96:97], v[26:27], v[144:145], v[96:97] op_sel:[1,0,0]
	v_pk_fma_f32 v[98:99], v[26:27], v[146:147], v[98:99] op_sel:[1,0,0]
	v_pk_fma_f32 v[100:101], v[42:43], v[132:133], v[100:101] op_sel:[1,0,0]
	v_pk_fma_f32 v[102:103], v[42:43], v[134:135], v[102:103] op_sel:[1,0,0]
	v_pk_fma_f32 v[104:105], v[42:43], v[136:137], v[104:105] op_sel:[1,0,0]
	v_pk_fma_f32 v[106:107], v[42:43], v[138:139], v[106:107] op_sel:[1,0,0]
	v_pk_fma_f32 v[108:109], v[42:43], v[140:141], v[108:109] op_sel:[1,0,0]
	v_pk_fma_f32 v[110:111], v[42:43], v[142:143], v[110:111] op_sel:[1,0,0]
	v_pk_fma_f32 v[112:113], v[42:43], v[144:145], v[112:113] op_sel:[1,0,0]
	v_pk_fma_f32 v[114:115], v[42:43], v[146:147], v[114:115] op_sel:[1,0,0]
	ds_read_b128 v[132:135], v231 offset:40960
	ds_read_b128 v[136:139], v231 offset:41984
	ds_read_b128 v[140:143], v231 offset:43008
	ds_read_b128 v[144:147], v231 offset:44032
	s_waitcnt lgkmcnt(8)
	v_pk_fma_f32 v[84:85], v[28:29], v[148:149], v[84:85] op_sel_hi:[0,1,1]
	v_pk_fma_f32 v[86:87], v[28:29], v[150:151], v[86:87] op_sel_hi:[0,1,1]
	v_pk_fma_f32 v[88:89], v[28:29], v[152:153], v[88:89] op_sel_hi:[0,1,1]
	v_pk_fma_f32 v[90:91], v[28:29], v[154:155], v[90:91] op_sel_hi:[0,1,1]
	v_pk_fma_f32 v[92:93], v[28:29], v[156:157], v[92:93] op_sel_hi:[0,1,1]
	v_pk_fma_f32 v[94:95], v[28:29], v[158:159], v[94:95] op_sel_hi:[0,1,1]
	v_pk_fma_f32 v[96:97], v[28:29], v[160:161], v[96:97] op_sel_hi:[0,1,1]
	v_pk_fma_f32 v[98:99], v[28:29], v[162:163], v[98:99] op_sel_hi:[0,1,1]
	v_pk_fma_f32 v[100:101], v[44:45], v[148:149], v[100:101] op_sel_hi:[0,1,1]
	v_pk_fma_f32 v[102:103], v[44:45], v[150:151], v[102:103] op_sel_hi:[0,1,1]
	v_pk_fma_f32 v[104:105], v[44:45], v[152:153], v[104:105] op_sel_hi:[0,1,1]
	v_pk_fma_f32 v[106:107], v[44:45], v[154:155], v[106:107] op_sel_hi:[0,1,1]
	v_pk_fma_f32 v[108:109], v[44:45], v[156:157], v[108:109] op_sel_hi:[0,1,1]
	v_pk_fma_f32 v[110:111], v[44:45], v[158:159], v[110:111] op_sel_hi:[0,1,1]
	v_pk_fma_f32 v[112:113], v[44:45], v[160:161], v[112:113] op_sel_hi:[0,1,1]
	v_pk_fma_f32 v[114:115], v[44:45], v[162:163], v[114:115] op_sel_hi:[0,1,1]
	ds_read_b128 v[148:151], v231 offset:45056
	ds_read_b128 v[152:155], v231 offset:46080
	ds_read_b128 v[156:159], v231 offset:47104
	ds_read_b128 v[160:163], v231 offset:48128
	s_waitcnt lgkmcnt(8)
	v_pk_fma_f32 v[84:85], v[28:29], v[116:117], v[84:85] op_sel:[1,0,0]
	v_pk_fma_f32 v[86:87], v[28:29], v[118:119], v[86:87] op_sel:[1,0,0]
	v_pk_fma_f32 v[88:89], v[28:29], v[120:121], v[88:89] op_sel:[1,0,0]
	v_pk_fma_f32 v[90:91], v[28:29], v[122:123], v[90:91] op_sel:[1,0,0]
	v_pk_fma_f32 v[92:93], v[28:29], v[124:125], v[92:93] op_sel:[1,0,0]
	v_pk_fma_f32 v[94:95], v[28:29], v[126:127], v[94:95] op_sel:[1,0,0]
	v_pk_fma_f32 v[96:97], v[28:29], v[128:129], v[96:97] op_sel:[1,0,0]
	v_pk_fma_f32 v[98:99], v[28:29], v[130:131], v[98:99] op_sel:[1,0,0]
	v_pk_fma_f32 v[100:101], v[44:45], v[116:117], v[100:101] op_sel:[1,0,0]
	v_pk_fma_f32 v[102:103], v[44:45], v[118:119], v[102:103] op_sel:[1,0,0]
	v_pk_fma_f32 v[104:105], v[44:45], v[120:121], v[104:105] op_sel:[1,0,0]
	v_pk_fma_f32 v[106:107], v[44:45], v[122:123], v[106:107] op_sel:[1,0,0]
	v_pk_fma_f32 v[108:109], v[44:45], v[124:125], v[108:109] op_sel:[1,0,0]
	v_pk_fma_f32 v[110:111], v[44:45], v[126:127], v[110:111] op_sel:[1,0,0]
	v_pk_fma_f32 v[112:113], v[44:45], v[128:129], v[112:113] op_sel:[1,0,0]
	v_pk_fma_f32 v[114:115], v[44:45], v[130:131], v[114:115] op_sel:[1,0,0]
	ds_read_b128 v[116:119], v231 offset:49152
	ds_read_b128 v[120:123], v231 offset:50176
	ds_read_b128 v[124:127], v231 offset:51200
	ds_read_b128 v[128:131], v231 offset:52224
	s_waitcnt lgkmcnt(8)
	v_pk_fma_f32 v[84:85], v[30:31], v[132:133], v[84:85] op_sel_hi:[0,1,1]
	v_pk_fma_f32 v[86:87], v[30:31], v[134:135], v[86:87] op_sel_hi:[0,1,1]
	v_pk_fma_f32 v[88:89], v[30:31], v[136:137], v[88:89] op_sel_hi:[0,1,1]
	v_pk_fma_f32 v[90:91], v[30:31], v[138:139], v[90:91] op_sel_hi:[0,1,1]
	v_pk_fma_f32 v[92:93], v[30:31], v[140:141], v[92:93] op_sel_hi:[0,1,1]
	v_pk_fma_f32 v[94:95], v[30:31], v[142:143], v[94:95] op_sel_hi:[0,1,1]
	v_pk_fma_f32 v[96:97], v[30:31], v[144:145], v[96:97] op_sel_hi:[0,1,1]
	v_pk_fma_f32 v[98:99], v[30:31], v[146:147], v[98:99] op_sel_hi:[0,1,1]
	v_pk_fma_f32 v[100:101], v[46:47], v[132:133], v[100:101] op_sel_hi:[0,1,1]
	v_pk_fma_f32 v[102:103], v[46:47], v[134:135], v[102:103] op_sel_hi:[0,1,1]
	v_pk_fma_f32 v[104:105], v[46:47], v[136:137], v[104:105] op_sel_hi:[0,1,1]
	v_pk_fma_f32 v[106:107], v[46:47], v[138:139], v[106:107] op_sel_hi:[0,1,1]
	v_pk_fma_f32 v[108:109], v[46:47], v[140:141], v[108:109] op_sel_hi:[0,1,1]
	v_pk_fma_f32 v[110:111], v[46:47], v[142:143], v[110:111] op_sel_hi:[0,1,1]
	v_pk_fma_f32 v[112:113], v[46:47], v[144:145], v[112:113] op_sel_hi:[0,1,1]
	v_pk_fma_f32 v[114:115], v[46:47], v[146:147], v[114:115] op_sel_hi:[0,1,1]
	ds_read_b128 v[132:135], v231 offset:53248
	ds_read_b128 v[136:139], v231 offset:54272
	ds_read_b128 v[140:143], v231 offset:55296
	ds_read_b128 v[144:147], v231 offset:56320
	s_waitcnt lgkmcnt(8)
	v_pk_fma_f32 v[84:85], v[30:31], v[148:149], v[84:85] op_sel:[1,0,0]
	v_pk_fma_f32 v[86:87], v[30:31], v[150:151], v[86:87] op_sel:[1,0,0]
	v_pk_fma_f32 v[88:89], v[30:31], v[152:153], v[88:89] op_sel:[1,0,0]
	v_pk_fma_f32 v[90:91], v[30:31], v[154:155], v[90:91] op_sel:[1,0,0]
	v_pk_fma_f32 v[92:93], v[30:31], v[156:157], v[92:93] op_sel:[1,0,0]
	v_pk_fma_f32 v[94:95], v[30:31], v[158:159], v[94:95] op_sel:[1,0,0]
	v_pk_fma_f32 v[96:97], v[30:31], v[160:161], v[96:97] op_sel:[1,0,0]
	v_pk_fma_f32 v[98:99], v[30:31], v[162:163], v[98:99] op_sel:[1,0,0]
	v_pk_fma_f32 v[100:101], v[46:47], v[148:149], v[100:101] op_sel:[1,0,0]
	v_pk_fma_f32 v[102:103], v[46:47], v[150:151], v[102:103] op_sel:[1,0,0]
	v_pk_fma_f32 v[104:105], v[46:47], v[152:153], v[104:105] op_sel:[1,0,0]
	v_pk_fma_f32 v[106:107], v[46:47], v[154:155], v[106:107] op_sel:[1,0,0]
	v_pk_fma_f32 v[108:109], v[46:47], v[156:157], v[108:109] op_sel:[1,0,0]
	v_pk_fma_f32 v[110:111], v[46:47], v[158:159], v[110:111] op_sel:[1,0,0]
	v_pk_fma_f32 v[112:113], v[46:47], v[160:161], v[112:113] op_sel:[1,0,0]
	v_pk_fma_f32 v[114:115], v[46:47], v[162:163], v[114:115] op_sel:[1,0,0]
	ds_read_b128 v[148:151], v231 offset:57344
	ds_read_b128 v[152:155], v231 offset:58368
	ds_read_b128 v[156:159], v231 offset:59392
	ds_read_b128 v[160:163], v231 offset:60416
	s_waitcnt lgkmcnt(8)
	v_pk_fma_f32 v[84:85], v[32:33], v[116:117], v[84:85] op_sel_hi:[0,1,1]
	v_pk_fma_f32 v[86:87], v[32:33], v[118:119], v[86:87] op_sel_hi:[0,1,1]
	v_pk_fma_f32 v[88:89], v[32:33], v[120:121], v[88:89] op_sel_hi:[0,1,1]
	v_pk_fma_f32 v[90:91], v[32:33], v[122:123], v[90:91] op_sel_hi:[0,1,1]
	v_pk_fma_f32 v[92:93], v[32:33], v[124:125], v[92:93] op_sel_hi:[0,1,1]
	v_pk_fma_f32 v[94:95], v[32:33], v[126:127], v[94:95] op_sel_hi:[0,1,1]
	v_pk_fma_f32 v[96:97], v[32:33], v[128:129], v[96:97] op_sel_hi:[0,1,1]
	v_pk_fma_f32 v[98:99], v[32:33], v[130:131], v[98:99] op_sel_hi:[0,1,1]
	v_pk_fma_f32 v[100:101], v[48:49], v[116:117], v[100:101] op_sel_hi:[0,1,1]
	v_pk_fma_f32 v[102:103], v[48:49], v[118:119], v[102:103] op_sel_hi:[0,1,1]
	v_pk_fma_f32 v[104:105], v[48:49], v[120:121], v[104:105] op_sel_hi:[0,1,1]
	v_pk_fma_f32 v[106:107], v[48:49], v[122:123], v[106:107] op_sel_hi:[0,1,1]
	v_pk_fma_f32 v[108:109], v[48:49], v[124:125], v[108:109] op_sel_hi:[0,1,1]
	v_pk_fma_f32 v[110:111], v[48:49], v[126:127], v[110:111] op_sel_hi:[0,1,1]
	v_pk_fma_f32 v[112:113], v[48:49], v[128:129], v[112:113] op_sel_hi:[0,1,1]
	v_pk_fma_f32 v[114:115], v[48:49], v[130:131], v[114:115] op_sel_hi:[0,1,1]
	ds_read_b128 v[116:119], v231 offset:61440
	ds_read_b128 v[120:123], v231 offset:62464
	ds_read_b128 v[124:127], v231 offset:63488
	ds_read_b128 v[128:131], v231 offset:64512
	s_waitcnt lgkmcnt(8)
	v_pk_fma_f32 v[84:85], v[32:33], v[132:133], v[84:85] op_sel:[1,0,0]
	v_pk_fma_f32 v[86:87], v[32:33], v[134:135], v[86:87] op_sel:[1,0,0]
	v_pk_fma_f32 v[88:89], v[32:33], v[136:137], v[88:89] op_sel:[1,0,0]
	v_pk_fma_f32 v[90:91], v[32:33], v[138:139], v[90:91] op_sel:[1,0,0]
	v_pk_fma_f32 v[92:93], v[32:33], v[140:141], v[92:93] op_sel:[1,0,0]
	v_pk_fma_f32 v[94:95], v[32:33], v[142:143], v[94:95] op_sel:[1,0,0]
	v_pk_fma_f32 v[96:97], v[32:33], v[144:145], v[96:97] op_sel:[1,0,0]
	v_pk_fma_f32 v[98:99], v[32:33], v[146:147], v[98:99] op_sel:[1,0,0]
	v_pk_fma_f32 v[100:101], v[48:49], v[132:133], v[100:101] op_sel:[1,0,0]
	v_pk_fma_f32 v[102:103], v[48:49], v[134:135], v[102:103] op_sel:[1,0,0]
	v_pk_fma_f32 v[104:105], v[48:49], v[136:137], v[104:105] op_sel:[1,0,0]
	v_pk_fma_f32 v[106:107], v[48:49], v[138:139], v[106:107] op_sel:[1,0,0]
	v_pk_fma_f32 v[108:109], v[48:49], v[140:141], v[108:109] op_sel:[1,0,0]
	v_pk_fma_f32 v[110:111], v[48:49], v[142:143], v[110:111] op_sel:[1,0,0]
	v_pk_fma_f32 v[112:113], v[48:49], v[144:145], v[112:113] op_sel:[1,0,0]
	v_pk_fma_f32 v[114:115], v[48:49], v[146:147], v[114:115] op_sel:[1,0,0]
	s_waitcnt lgkmcnt(4)
	v_pk_fma_f32 v[84:85], v[34:35], v[148:149], v[84:85] op_sel_hi:[0,1,1]
	v_pk_fma_f32 v[86:87], v[34:35], v[150:151], v[86:87] op_sel_hi:[0,1,1]
	v_pk_fma_f32 v[88:89], v[34:35], v[152:153], v[88:89] op_sel_hi:[0,1,1]
	v_pk_fma_f32 v[90:91], v[34:35], v[154:155], v[90:91] op_sel_hi:[0,1,1]
	v_pk_fma_f32 v[92:93], v[34:35], v[156:157], v[92:93] op_sel_hi:[0,1,1]
	v_pk_fma_f32 v[94:95], v[34:35], v[158:159], v[94:95] op_sel_hi:[0,1,1]
	v_pk_fma_f32 v[96:97], v[34:35], v[160:161], v[96:97] op_sel_hi:[0,1,1]
	v_pk_fma_f32 v[98:99], v[34:35], v[162:163], v[98:99] op_sel_hi:[0,1,1]
	v_pk_fma_f32 v[100:101], v[50:51], v[148:149], v[100:101] op_sel_hi:[0,1,1]
	v_pk_fma_f32 v[102:103], v[50:51], v[150:151], v[102:103] op_sel_hi:[0,1,1]
	v_pk_fma_f32 v[104:105], v[50:51], v[152:153], v[104:105] op_sel_hi:[0,1,1]
	v_pk_fma_f32 v[106:107], v[50:51], v[154:155], v[106:107] op_sel_hi:[0,1,1]
	v_pk_fma_f32 v[108:109], v[50:51], v[156:157], v[108:109] op_sel_hi:[0,1,1]
	v_pk_fma_f32 v[110:111], v[50:51], v[158:159], v[110:111] op_sel_hi:[0,1,1]
	v_pk_fma_f32 v[112:113], v[50:51], v[160:161], v[112:113] op_sel_hi:[0,1,1]
	v_pk_fma_f32 v[114:115], v[50:51], v[162:163], v[114:115] op_sel_hi:[0,1,1]
	s_waitcnt lgkmcnt(0)
	v_pk_fma_f32 v[84:85], v[34:35], v[116:117], v[84:85] op_sel:[1,0,0]
	v_pk_fma_f32 v[86:87], v[34:35], v[118:119], v[86:87] op_sel:[1,0,0]
	v_pk_fma_f32 v[88:89], v[34:35], v[120:121], v[88:89] op_sel:[1,0,0]
	v_pk_fma_f32 v[90:91], v[34:35], v[122:123], v[90:91] op_sel:[1,0,0]
	v_pk_fma_f32 v[92:93], v[34:35], v[124:125], v[92:93] op_sel:[1,0,0]
	v_pk_fma_f32 v[94:95], v[34:35], v[126:127], v[94:95] op_sel:[1,0,0]
	v_pk_fma_f32 v[96:97], v[34:35], v[128:129], v[96:97] op_sel:[1,0,0]
	v_pk_fma_f32 v[98:99], v[34:35], v[130:131], v[98:99] op_sel:[1,0,0]
	v_pk_fma_f32 v[100:101], v[50:51], v[116:117], v[100:101] op_sel:[1,0,0]
	v_pk_fma_f32 v[102:103], v[50:51], v[118:119], v[102:103] op_sel:[1,0,0]
	v_pk_fma_f32 v[104:105], v[50:51], v[120:121], v[104:105] op_sel:[1,0,0]
	v_pk_fma_f32 v[106:107], v[50:51], v[122:123], v[106:107] op_sel:[1,0,0]
	v_pk_fma_f32 v[108:109], v[50:51], v[124:125], v[108:109] op_sel:[1,0,0]
	v_pk_fma_f32 v[110:111], v[50:51], v[126:127], v[110:111] op_sel:[1,0,0]
	v_pk_fma_f32 v[112:113], v[50:51], v[128:129], v[112:113] op_sel:[1,0,0]
	v_pk_fma_f32 v[114:115], v[50:51], v[130:131], v[114:115] op_sel:[1,0,0]
	v_permlane32_swap_b32_e32 v84, v92
	v_permlane32_swap_b32_e32 v100, v108
	v_permlane32_swap_b32_e32 v85, v93
	v_permlane32_swap_b32_e32 v101, v109
	v_permlane32_swap_b32_e32 v86, v94
	v_permlane32_swap_b32_e32 v102, v110
	v_permlane32_swap_b32_e32 v87, v95
	v_permlane32_swap_b32_e32 v103, v111
	v_permlane32_swap_b32_e32 v88, v96
	v_permlane32_swap_b32_e32 v104, v112
	v_permlane32_swap_b32_e32 v89, v97
	v_permlane32_swap_b32_e32 v105, v113
	v_permlane32_swap_b32_e32 v90, v98
	v_permlane32_swap_b32_e32 v106, v114
	v_permlane32_swap_b32_e32 v91, v99
	v_permlane32_swap_b32_e32 v107, v115
	v_add_f32_e32 v84, v84, v92
	v_add_f32_e32 v100, v100, v108
	v_add_f32_e32 v85, v85, v93
	v_add_f32_e32 v101, v101, v109
	v_add_f32_e32 v86, v86, v94
	v_add_f32_e32 v102, v102, v110
	v_add_f32_e32 v87, v87, v95
	v_add_f32_e32 v103, v103, v111
	v_add_f32_e32 v88, v88, v96
	v_add_f32_e32 v104, v104, v112
	v_add_f32_e32 v89, v89, v97
	v_add_f32_e32 v105, v105, v113
	v_add_f32_e32 v90, v90, v98
	v_add_f32_e32 v106, v106, v114
	v_add_f32_e32 v91, v91, v99
	v_add_f32_e32 v107, v107, v115
	v_permlane16_swap_b32_e32 v84, v88
	v_permlane16_swap_b32_e32 v100, v104
	v_permlane16_swap_b32_e32 v85, v89
	v_permlane16_swap_b32_e32 v101, v105
	v_permlane16_swap_b32_e32 v86, v90
	v_permlane16_swap_b32_e32 v102, v106
	v_permlane16_swap_b32_e32 v87, v91
	v_permlane16_swap_b32_e32 v103, v107
	v_add_f32_e32 v84, v84, v88
	v_add_f32_e32 v100, v100, v104
	v_add_f32_e32 v85, v85, v89
	v_add_f32_e32 v101, v101, v105
	v_add_f32_e32 v86, v86, v90
	v_add_f32_e32 v102, v102, v106
	v_add_f32_e32 v87, v87, v91
	v_add_f32_e32 v103, v103, v107
	v_cndmask_b32_e64 v88, v86, v84, s[26:27]
	v_cndmask_b32_e64 v89, v87, v85, s[26:27]
	v_cndmask_b32_e64 v104, v102, v100, s[26:27]
	v_cndmask_b32_e64 v105, v103, v101, s[26:27]
	v_cndmask_b32_e64 v84, v84, v86, s[26:27]
	v_cndmask_b32_e64 v85, v85, v87, s[26:27]
	v_cndmask_b32_e64 v100, v100, v102, s[26:27]
	v_cndmask_b32_e64 v101, v101, v103, s[26:27]
	v_add_f32_dpp v84, v84, v88 row_ror:8 row_mask:0xf bank_mask:0xf bound_ctrl:1
	v_add_f32_dpp v100, v100, v104 row_ror:8 row_mask:0xf bank_mask:0xf bound_ctrl:1
	v_add_f32_dpp v85, v85, v89 row_ror:8 row_mask:0xf bank_mask:0xf bound_ctrl:1
	v_add_f32_dpp v101, v101, v105 row_ror:8 row_mask:0xf bank_mask:0xf bound_ctrl:1
	v_cndmask_b32_e64 v86, v85, v84, s[28:29]
	v_cndmask_b32_e64 v102, v101, v100, s[28:29]
	v_cndmask_b32_e64 v84, v84, v85, s[28:29]
	v_cndmask_b32_e64 v100, v100, v101, s[28:29]
	s_nop 0
	v_add_f32_dpp v84, v84, v86 row_half_mirror row_mask:0xf bank_mask:0xf bound_ctrl:1
	v_add_f32_dpp v100, v100, v102 row_half_mirror row_mask:0xf bank_mask:0xf bound_ctrl:1
	s_nop 0
	v_add_f32_dpp v84, v84, v84 quad_perm:[1,0,3,2] row_mask:0xf bank_mask:0xf bound_ctrl:1
	v_add_f32_dpp v100, v100, v100 quad_perm:[1,0,3,2] row_mask:0xf bank_mask:0xf bound_ctrl:1
	s_nop 0
	v_add_f32_dpp v84, v84, v84 quad_perm:[2,3,0,1] row_mask:0xf bank_mask:0xf bound_ctrl:1
	v_add_f32_dpp v100, v100, v100 quad_perm:[2,3,0,1] row_mask:0xf bank_mask:0xf bound_ctrl:1
	v_add_f32_e32 v84, v235, v84
	v_add_f32_e32 v100, v235, v100
	v_mov_b32_e32 v90, v84
	v_mov_b32_e32 v106, v100
	v_mov_b32_e32 v91, v84
	v_mov_b32_e32 v107, v100
	s_nop 0
	v_permlane32_swap_b32_e32 v90, v91
	v_permlane32_swap_b32_e32 v106, v107
	v_max_f32_e32 v90, v90, v91
	v_max_f32_e32 v106, v106, v107
	v_mov_b32_e32 v91, v90
	v_mov_b32_e32 v107, v106
	s_nop 0
	v_permlane16_swap_b32_e32 v90, v91
	v_permlane16_swap_b32_e32 v106, v107
	v_max_f32_e32 v90, v90, v91
	v_max_f32_e32 v106, v106, v107
	s_nop 0
	v_max_f32_dpp v90, v90, v90 row_ror:8 row_mask:0xf bank_mask:0xf bound_ctrl:1
	v_max_f32_dpp v106, v106, v106 row_ror:8 row_mask:0xf bank_mask:0xf bound_ctrl:1
	s_nop 0
	v_max_f32_dpp v90, v90, v90 row_half_mirror row_mask:0xf bank_mask:0xf bound_ctrl:1
	v_max_f32_dpp v106, v106, v106 row_half_mirror row_mask:0xf bank_mask:0xf bound_ctrl:1
	v_sub_f32_e32 v92, v84, v90
	v_sub_f32_e32 v108, v100, v106
	v_mul_f32_e32 v92, 0x3fb8aa3b, v92
	v_mul_f32_e32 v108, 0x3fb8aa3b, v108
	v_exp_f32_e32 v92, v92
	v_exp_f32_e32 v108, v108
	v_mov_b32_e32 v93, v92
	v_mov_b32_e32 v109, v108
	v_mov_b32_e32 v94, v92
	v_mov_b32_e32 v110, v108
	s_nop 0
	v_permlane32_swap_b32_e32 v93, v94
	v_permlane32_swap_b32_e32 v109, v110
	v_add_f32_e32 v93, v93, v94
	v_add_f32_e32 v109, v109, v110
	v_mov_b32_e32 v94, v93
	v_mov_b32_e32 v110, v109
	s_nop 0
	v_permlane16_swap_b32_e32 v93, v94
	v_permlane16_swap_b32_e32 v109, v110
	v_add_f32_e32 v93, v93, v94
	v_add_f32_e32 v109, v109, v110
	s_nop 0
	v_add_f32_dpp v93, v93, v93 row_ror:8 row_mask:0xf bank_mask:0xf bound_ctrl:1
	v_add_f32_dpp v109, v109, v109 row_ror:8 row_mask:0xf bank_mask:0xf bound_ctrl:1
	s_nop 0
	v_add_f32_dpp v93, v93, v93 row_half_mirror row_mask:0xf bank_mask:0xf bound_ctrl:1
	v_add_f32_dpp v109, v109, v109 row_half_mirror row_mask:0xf bank_mask:0xf bound_ctrl:1
	v_rcp_f32_e32 v96, v93
	v_rcp_f32_e32 v112, v109
	v_mul_f32_e32 v95, v92, v96
	v_mul_f32_e32 v111, v108, v112
	v_fma_f32 v97, -v93, v95, v92
	v_fma_f32 v113, -v109, v111, v108
	v_fma_f32 v95, v97, v96, v95
	v_fma_f32 v111, v113, v112, v111
	s_mov_b64 exec, s[30:31]
	global_store_dword v232, v95, s[8:9]
	global_store_dword v237, v111, s[8:9]
	s_mov_b64 exec, -1
	s_add_i32 s23, s21, 1
	s_lshl_b32 s0, s23, 11
	s_lshl_b32 s1, s23, 6
	s_add_u32 s6, s6, s0
	s_addc_u32 s7, s7, 0
	s_add_u32 s8, s8, s1
	s_addc_u32 s9, s9, 0
	s_mov_b32 s18, s36
	s_mov_b32 s21, s37
	s_lshl_b32 s0, s37, 11
	s_lshl_b32 s1, s37, 6
	v_add_u32_e32 v238, s0, v230
	v_add_u32_e32 v237, s1, v232
	s_cmp_lt_i32 s18, s19
	s_cbranch_scc1 .Ln2_loop
	s_waitcnt lgkmcnt(0)
	s_branch .Ln2_done
.Ln2_reload:
	s_mov_b32 s20, s23
	s_mul_i32 s0, s23, s22
	s_add_u32 s0, s10, s0
	s_addc_u32 s1, s11, 0
	s_add_u32 s0, s0, 0x3000
	s_addc_u32 s1, s1, 0
	global_load_dwordx4 v[68:71], v231, s[0:1] offset:0
	global_load_dwordx4 v[72:75], v231, s[0:1] offset:1024
	global_load_dwordx4 v[76:79], v231, s[0:1] offset:2048
	global_load_dwordx4 v[80:83], v231, s[0:1] offset:3072
	s_add_u32 s0, s0, 0x1000
	s_addc_u32 s1, s1, 0
	global_load_dwordx4 v[52:55], v231, s[0:1] offset:0
	global_load_dwordx4 v[56:59], v231, s[0:1] offset:1024
	global_load_dwordx4 v[60:63], v231, s[0:1] offset:2048
	global_load_dwordx4 v[64:67], v231, s[0:1] offset:3072
	s_waitcnt vmcnt(0)
	v_add_f32_e32 v52, 1.0, v52
	v_add_f32_e32 v53, 1.0, v53
	v_add_f32_e32 v54, 1.0, v54
	v_add_f32_e32 v55, 1.0, v55
	v_add_f32_e32 v56, 1.0, v56
	v_add_f32_e32 v57, 1.0, v57
	v_add_f32_e32 v58, 1.0, v58
	v_add_f32_e32 v59, 1.0, v59
	v_add_f32_e32 v60, 1.0, v60
	v_add_f32_e32 v61, 1.0, v61
	v_add_f32_e32 v62, 1.0, v62
	v_add_f32_e32 v63, 1.0, v63
	v_add_f32_e32 v64, 1.0, v64
	v_add_f32_e32 v65, 1.0, v65
	v_add_f32_e32 v66, 1.0, v66
	v_add_f32_e32 v67, 1.0, v67
	v_mul_f32_e32 v52, v172, v52
	v_mul_f32_e32 v53, v173, v53
	v_mul_f32_e32 v54, v174, v54
	v_mul_f32_e32 v55, v175, v55
	v_mul_f32_e32 v56, v176, v56
	v_mul_f32_e32 v57, v177, v57
	v_mul_f32_e32 v58, v178, v58
	v_mul_f32_e32 v59, v179, v59
	v_mul_f32_e32 v60, v180, v60
	v_mul_f32_e32 v61, v181, v61
	v_mul_f32_e32 v62, v182, v62
	v_mul_f32_e32 v63, v183, v63
	v_mul_f32_e32 v64, v184, v64
	v_mul_f32_e32 v65, v185, v65
	v_mul_f32_e32 v66, v186, v66
	v_mul_f32_e32 v67, v187, v67
	s_branch .Ln2_reload_back
.Ln2_done:
.LBB0_1057:
	s_or_b64 exec, exec, s[14:15]
	s_barrier
	s_waitcnt vmcnt(0)
	s_barrier
	s_and_saveexec_b64 s[0:1], s[80:81]
	s_cbranch_execz .LBB0_1109
	v_readlane_b32 s4, v255, 8
	s_mov_b32 s10, s74
	s_waitcnt vmcnt(0) expcnt(0) lgkmcnt(0)
	v_mov_b32_e32 v2, s4
	ds_read_b32 v4, v2
	v_readlane_b32 s4, v255, 9
	s_waitcnt lgkmcnt(0)
	v_cmp_ne_u32_e32 vcc, 0, v4
	v_mov_b32_e32 v2, s4
	ds_read_b32 v2, v2
	s_cbranch_vccnz .LBB0_1073
	v_readlane_b32 s6, v255, 0
	v_readlane_b32 s7, v255, 1
	s_load_dwordx2 s[4:5], s[6:7], 0x4
	s_mov_b32 s12, 1
	s_waitcnt lgkmcnt(0)
	s_mul_i32 s11, s4, s79
	s_mul_i32 s11, s11, s5
	s_branch .LBB0_1061
